# v23 + cross-half row-max exchange via v_permlane32_swap on a copy instead of ds_bpermute LDS round trip (6 attention sites)
# speedup vs baseline: 1.0094x; 1.0046x over previous
.LBB0_719:
	s_mul_i32 s26, s64, 0x5400
	v_add_u32_e32 v2, s26, v205
	s_waitcnt lgkmcnt(3)
	ds_read_b128 v[4:7], v2
	s_waitcnt lgkmcnt(1)
	ds_read_b128 v[8:11], v2 offset:32
	ds_read_b128 v[12:15], v2 offset:6656
	ds_read_b128 v[82:85], v2 offset:6688
	ds_read_b128 v[158:161], v2 offset:64
	ds_read_b128 v[162:165], v2 offset:96
	ds_read_b128 v[86:89], v2 offset:6720
	ds_read_b128 v[90:93], v2 offset:6752
	ds_read_b128 v[194:197], v2 offset:128
	ds_read_b128 v[208:211], v2 offset:160
	ds_read_b128 v[94:97], v2 offset:6784
	ds_read_b128 v[166:169], v2 offset:6816
	v_add_u32_e32 v2, s26, v206
	s_waitcnt lgkmcnt(9)
	v_mfma_f32_32x32x16_bf16 v[66:81], v[12:15], v[134:137], v[50:65]
	s_waitcnt lgkmcnt(8)
	v_mfma_f32_32x32x16_bf16 v[66:81], v[82:85], v[138:141], v[66:81]
	s_waitcnt lgkmcnt(5)
	v_mfma_f32_32x32x16_bf16 v[66:81], v[86:89], v[142:145], v[66:81]
	s_waitcnt lgkmcnt(4)
	v_mfma_f32_32x32x16_bf16 v[66:81], v[90:93], v[146:149], v[66:81]
	s_waitcnt lgkmcnt(1)
	v_mfma_f32_32x32x16_bf16 v[66:81], v[94:97], v[150:153], v[66:81]
	s_waitcnt lgkmcnt(0)
	v_mfma_f32_32x32x16_bf16 v[66:81], v[166:169], v[154:157], v[66:81]
	v_mfma_f32_32x32x16_bf16 v[82:97], v[4:7], v[134:137], v[50:65]
	v_mfma_f32_32x32x16_bf16 v[82:97], v[8:11], v[138:141], v[82:97]
	ds_read_b64_tr_b16 v[174:175], v2 offset:13312
	ds_read_b64_tr_b16 v[176:177], v2 offset:13824
	ds_read_b64_tr_b16 v[170:171], v2 offset:14336
	ds_read_b64_tr_b16 v[172:173], v2 offset:14848
	ds_read_b64_tr_b16 v[166:167], v2 offset:15360
	ds_read_b64_tr_b16 v[168:169], v2 offset:15872
	ds_read_b64_tr_b16 v[8:9], v2 offset:16384
	ds_read_b64_tr_b16 v[10:11], v2 offset:16896
	v_mfma_f32_32x32x16_bf16 v[82:97], v[158:161], v[142:145], v[82:97]
	v_mfma_f32_32x32x16_bf16 v[82:97], v[162:165], v[146:149], v[82:97]
	ds_read_b64_tr_b16 v[162:163], v2 offset:17408
	ds_read_b64_tr_b16 v[164:165], v2 offset:17920
	ds_read_b64_tr_b16 v[158:159], v2 offset:18432
	ds_read_b64_tr_b16 v[160:161], v2 offset:18944
	ds_read_b64_tr_b16 v[12:13], v2 offset:19456
	ds_read_b64_tr_b16 v[14:15], v2 offset:19968
	ds_read_b64_tr_b16 v[4:5], v2 offset:20480
	ds_read_b64_tr_b16 v[6:7], v2 offset:20992
	v_mfma_f32_32x32x16_bf16 v[82:97], v[194:197], v[150:153], v[82:97]
	v_mfma_f32_32x32x16_bf16 v[82:97], v[208:211], v[154:157], v[82:97]
	s_nop 4
	v_max3_f32 v194, v66, v67, v68
	v_max3_f32 v196, v69, v70, v71
	v_max3_f32 v194, v194, v72, v73
	v_max3_f32 v196, v196, v74, v75
	v_max3_f32 v194, v194, v76, v77
	v_max3_f32 v196, v196, v78, v79
	v_max3_f32 v194, v194, v196, v80
	v_max3_f32 v2, v82, v83, v84
	v_max3_f32 v195, v85, v86, v87
	v_max3_f32 v2, v2, v88, v89
	v_max3_f32 v195, v195, v90, v91
	v_max3_f32 v2, v2, v92, v93
	v_max3_f32 v195, v195, v94, v95
	v_max3_f32 v2, v2, v195, v96
	v_max_f32_e32 v195, v97, v81
	v_max3_f32 v2, v2, v194, v195
	v_mov_b32_e32 v194, v2
	s_cmp_lg_u32 s73, 0
	s_waitcnt lgkmcnt(0)
	s_nop 1
	v_permlane32_swap_b32_e32 v194, v2
	v_max_f32_e32 v208, v2, v194
	s_cbranch_scc0 .Lmla_f_first
	v_cmp_lt_f32_e32 vcc, s81, v208
	s_cbranch_vccz .LBB0_726
	v_max_f32_e32 v2, v208, v208
	v_max_f32_e32 v2, 0, v2
	s_branch .Lmla_f_resc

.LBB0_756:
	s_mul_i32 s26, s64, 0x5400
	v_add_u32_e32 v2, s26, v205
	s_waitcnt lgkmcnt(3)
	ds_read_b128 v[4:7], v2 offset:6656
	s_waitcnt lgkmcnt(1)
	ds_read_b128 v[8:11], v2
	ds_read_b128 v[12:15], v2 offset:32
	ds_read_b128 v[158:161], v2 offset:6688
	ds_read_b128 v[162:165], v2 offset:64
	ds_read_b128 v[166:169], v2 offset:6720
	ds_read_b128 v[170:173], v2 offset:96
	ds_read_b128 v[174:177], v2 offset:6752
	ds_read_b128 v[194:197], v2 offset:128
	ds_read_b128 v[210:213], v2 offset:6784
	ds_read_b128 v[214:217], v2 offset:160
	ds_read_b128 v[218:221], v2 offset:6816
	s_waitcnt lgkmcnt(10)
	v_mfma_f32_32x32x16_bf16 v[82:97], v[8:11], v[134:137], v[50:65]
	v_mfma_f32_32x32x16_bf16 v[66:81], v[4:7], v[134:137], v[50:65]
	v_add_u32_e32 v6, s26, v206
	s_waitcnt lgkmcnt(9)
	v_mfma_f32_32x32x16_bf16 v[82:97], v[12:15], v[138:141], v[82:97]
	s_waitcnt lgkmcnt(8)
	v_mfma_f32_32x32x16_bf16 v[66:81], v[158:161], v[138:141], v[66:81]
	s_waitcnt lgkmcnt(7)
	v_mfma_f32_32x32x16_bf16 v[82:97], v[162:165], v[142:145], v[82:97]
	s_waitcnt lgkmcnt(6)
	v_mfma_f32_32x32x16_bf16 v[66:81], v[166:169], v[142:145], v[66:81]
	s_waitcnt lgkmcnt(5)
	v_mfma_f32_32x32x16_bf16 v[82:97], v[170:173], v[146:149], v[82:97]
	s_waitcnt lgkmcnt(4)
	v_mfma_f32_32x32x16_bf16 v[66:81], v[174:177], v[146:149], v[66:81]
	ds_read_b64_tr_b16 v[174:175], v6 offset:13312
	ds_read_b64_tr_b16 v[176:177], v6 offset:13824
	ds_read_b64_tr_b16 v[170:171], v6 offset:14336
	ds_read_b64_tr_b16 v[172:173], v6 offset:14848
	ds_read_b64_tr_b16 v[166:167], v6 offset:15360
	ds_read_b64_tr_b16 v[168:169], v6 offset:15872
	ds_read_b64_tr_b16 v[162:163], v6 offset:16384
	ds_read_b64_tr_b16 v[164:165], v6 offset:16896
	ds_read_b64_tr_b16 v[158:159], v6 offset:17408
	ds_read_b64_tr_b16 v[160:161], v6 offset:17920
	ds_read_b64_tr_b16 v[12:13], v6 offset:18432
	ds_read_b64_tr_b16 v[14:15], v6 offset:18944
	ds_read_b64_tr_b16 v[8:9], v6 offset:19456
	ds_read_b64_tr_b16 v[10:11], v6 offset:19968
	ds_read_b64_tr_b16 v[4:5], v6 offset:20480
	ds_read_b64_tr_b16 v[6:7], v6 offset:20992
	s_waitcnt lgkmcnt(14)
	v_mfma_f32_32x32x16_bf16 v[82:97], v[194:197], v[150:153], v[82:97]
	v_mfma_f32_32x32x16_bf16 v[66:81], v[210:213], v[150:153], v[66:81]
	v_mfma_f32_32x32x16_bf16 v[82:97], v[214:217], v[154:157], v[82:97]
	v_mfma_f32_32x32x16_bf16 v[66:81], v[218:221], v[154:157], v[66:81]
	v_sub_u32_e32 v222, v208, v209
	v_add_u32_e32 v222, 59, v222
	s_cmp_lg_u32 s35, -1
	v_cmp_ge_i32_e64 vcc, v222, 32
	v_cmp_ge_i32_e64 s[28:29], v222, 1
	v_cmp_ge_i32_e64 s[30:31], v222, 0
	s_nop 5
	v_cndmask_b32_e64 v16, v243, v66, vcc
	v_cmp_ge_i32_e64 vcc, v222, 33
	v_cndmask_b32_e64 v83, v243, v83, s[28:29]
	v_cmp_ge_i32_e64 s[28:29], v222, 2
	v_cndmask_b32_e64 v82, v243, v82, s[30:31]
	v_cmp_ge_i32_e64 s[30:31], v222, 34
	v_cndmask_b32_e64 v17, v243, v67, vcc
	v_cmp_ge_i32_e64 vcc, v222, 3
	v_cndmask_b32_e64 v66, v243, v84, s[28:29]
	v_cmp_ge_i32_e64 s[28:29], v222, 35
	v_cndmask_b32_e64 v68, v243, v68, s[30:31]
	v_cmp_ge_i32_e64 s[30:31], v222, 8
	v_cndmask_b32_e64 v67, v243, v85, vcc
	v_cmp_ge_i32_e64 vcc, v222, 40
	v_cndmask_b32_e64 v69, v243, v69, s[28:29]
	v_cmp_ge_i32_e64 s[28:29], v222, 9
	v_cndmask_b32_e64 v84, v243, v86, s[30:31]
	v_cmp_ge_i32_e64 s[30:31], v222, 41
	v_cndmask_b32_e64 v70, v243, v70, vcc
	v_cmp_ge_i32_e64 vcc, v222, 10
	v_cndmask_b32_e64 v85, v243, v87, s[28:29]
	v_cmp_ge_i32_e64 s[28:29], v222, 42
	v_cndmask_b32_e64 v71, v243, v71, s[30:31]
	v_cmp_ge_i32_e64 s[30:31], v222, 11
	v_cndmask_b32_e64 v86, v243, v88, vcc
	v_cmp_ge_i32_e64 vcc, v222, 43
	v_cndmask_b32_e64 v72, v243, v72, s[28:29]
	v_cmp_ge_i32_e64 s[28:29], v222, 16
	v_cndmask_b32_e64 v87, v243, v89, s[30:31]
	v_cmp_ge_i32_e64 s[30:31], v222, 48
	v_cndmask_b32_e64 v73, v243, v73, vcc
	v_cmp_ge_i32_e64 vcc, v222, 17
	v_cndmask_b32_e64 v88, v243, v90, s[28:29]
	v_cmp_ge_i32_e64 s[28:29], v222, 49
	v_cndmask_b32_e64 v74, v243, v74, s[30:31]
	v_cmp_ge_i32_e64 s[30:31], v222, 18
	v_cndmask_b32_e64 v89, v243, v91, vcc
	v_cmp_ge_i32_e64 vcc, v222, 50
	v_cndmask_b32_e64 v75, v243, v75, s[28:29]
	v_cmp_ge_i32_e64 s[28:29], v222, 19
	v_cndmask_b32_e64 v90, v243, v92, s[30:31]
	v_cmp_ge_i32_e64 s[30:31], v222, 51
	v_cndmask_b32_e64 v76, v243, v76, vcc
	v_cmp_ge_i32_e64 vcc, v222, 24
	v_cndmask_b32_e64 v91, v243, v93, s[28:29]
	v_cmp_ge_i32_e64 s[28:29], v222, 56
	v_cndmask_b32_e64 v77, v243, v77, s[30:31]
	v_cmp_ge_i32_e64 s[30:31], v222, 25
	v_cndmask_b32_e64 v92, v243, v94, vcc
	v_cmp_ge_i32_e64 vcc, v222, 57
	v_cndmask_b32_e64 v78, v243, v78, s[28:29]
	v_cmp_ge_i32_e64 s[28:29], v222, 26
	v_cndmask_b32_e64 v93, v243, v95, s[30:31]
	v_cmp_ge_i32_e64 s[30:31], v222, 58
	v_cndmask_b32_e64 v79, v243, v79, vcc
	v_cmp_ge_i32_e64 vcc, v222, 27
	v_cndmask_b32_e64 v94, v243, v96, s[28:29]
	v_cmp_ge_i32_e64 s[28:29], v222, 59
	v_cndmask_b32_e64 v80, v243, v80, s[30:31]
	v_cndmask_b32_e64 v95, v243, v97, vcc
	v_cndmask_b32_e64 v81, v243, v81, s[28:29]
	v_max3_f32 v96, v16, v17, v68
	v_max3_f32 v2, v82, v83, v66
	v_max3_f32 v2, v2, v67, v84
	v_max3_f32 v96, v96, v69, v70
	v_max3_f32 v2, v2, v85, v86
	v_max3_f32 v96, v96, v71, v72
	v_max3_f32 v2, v2, v87, v88
	v_max3_f32 v96, v96, v73, v74
	v_max3_f32 v2, v2, v89, v90
	v_max3_f32 v96, v96, v75, v76
	v_max3_f32 v2, v2, v91, v92
	v_max3_f32 v96, v96, v77, v78
	v_max3_f32 v2, v2, v93, v94
	v_max3_f32 v96, v96, v79, v80
	v_max_f32_e32 v97, v95, v81
	v_max3_f32 v2, v2, v96, v97
	v_mov_b32_e32 v96, v2
	s_waitcnt lgkmcnt(0)
	s_nop 1
	v_permlane32_swap_b32_e32 v96, v2
	v_max_f32_e32 v96, v2, v96
	s_cbranch_scc0 .Lmla_m_first
	v_cmp_lt_f32_e32 vcc, s81, v96
	s_cbranch_vccz .LBB0_744
	v_max_f32_e32 v2, v96, v96
	v_max_f32_e32 v2, 0, v2
	s_branch .Lmla_m_resc

.LBB0_851:
	s_mul_i32 s2, s74, 0x4400
	s_add_i32 s6, s2, 0
	v_add_u32_e32 v5, s6, v207
	ds_read_b128 v[6:9], v5 offset:4608
	ds_read_b128 v[10:13], v5
	ds_read_b128 v[14:17], v5 offset:32
	ds_read_b128 v[146:149], v5 offset:4640
	s_cmp_lg_u32 s10, 0
	s_cselect_b64 s[2:3], -1, 0
	s_waitcnt lgkmcnt(2)
	v_mfma_f32_32x32x16_bf16 v[130:145], v[10:13], v[178:181], v[98:113]
	s_and_b64 vcc, exec, s[2:3]
	v_mfma_f32_32x32x16_bf16 v[114:129], v[6:9], v[178:181], v[98:113]
	s_waitcnt lgkmcnt(1)
	v_mfma_f32_32x32x16_bf16 v[130:145], v[14:17], v[182:185], v[130:145]
	s_waitcnt lgkmcnt(0)
	v_mfma_f32_32x32x16_bf16 v[114:129], v[146:149], v[182:185], v[114:129]
	s_nop 9
	v_max3_f32 v2, v130, v131, v132
	v_max3_f32 v8, v133, v134, v135
	v_max3_f32 v6, v114, v115, v116
	v_max3_f32 v7, v117, v118, v119
	v_max3_f32 v2, v2, v136, v137
	v_max3_f32 v8, v8, v138, v139
	v_max3_f32 v6, v6, v120, v121
	v_max3_f32 v7, v7, v122, v123
	v_max3_f32 v2, v2, v140, v141
	v_max3_f32 v8, v8, v142, v143
	v_max3_f32 v6, v6, v124, v125
	v_max3_f32 v7, v7, v126, v127
	v_max3_f32 v2, v2, v8, v144
	v_max3_f32 v6, v6, v7, v128
	v_max_f32_e32 v7, v145, v129
	v_max3_f32 v2, v2, v6, v7
	v_mov_b32_e32 v6, v2
	s_waitcnt lgkmcnt(0)
	s_nop 1
	v_permlane32_swap_b32_e32 v6, v2
	v_max_f32_e32 v6, v2, v6
	s_cbranch_vccz .Ldf0_first
	v_cmp_lt_f32_e32 vcc, s11, v6
	s_cbranch_vccz .LBB0_858
	v_max_f32_e32 v2, v6, v6
	v_max_f32_e32 v2, 0, v2
	s_branch .Ldf0_resc

.LBB0_858:
	ds_read_b128 v[6:9], v5 offset:64
	ds_read_b128 v[10:13], v5 offset:96
	ds_read_b128 v[14:17], v5 offset:4672
	ds_read_b128 v[194:197], v5 offset:4704
	s_waitcnt lgkmcnt(3)
	v_mfma_f32_32x32x16_bf16 v[162:177], v[6:9], v[186:189], v[82:97]
	s_and_b64 vcc, exec, s[2:3]
	s_waitcnt lgkmcnt(1)
	v_mfma_f32_32x32x16_bf16 v[146:161], v[14:17], v[186:189], v[82:97]
	v_mfma_f32_32x32x16_bf16 v[162:177], v[10:13], v[190:193], v[162:177]
	s_waitcnt lgkmcnt(0)
	v_mfma_f32_32x32x16_bf16 v[146:161], v[194:197], v[190:193], v[146:161]
	s_nop 9
	v_max3_f32 v2, v162, v163, v164
	v_max3_f32 v7, v165, v166, v167
	v_max3_f32 v5, v146, v147, v148
	v_max3_f32 v6, v149, v150, v151
	v_max3_f32 v2, v2, v168, v169
	v_max3_f32 v7, v7, v170, v171
	v_max3_f32 v5, v5, v152, v153
	v_max3_f32 v6, v6, v154, v155
	v_max3_f32 v2, v2, v172, v173
	v_max3_f32 v7, v7, v174, v175
	v_max3_f32 v5, v5, v156, v157
	v_max3_f32 v6, v6, v158, v159
	v_max3_f32 v2, v2, v7, v176
	v_max3_f32 v5, v5, v6, v160
	v_max_f32_e32 v6, v177, v161
	v_max3_f32 v2, v2, v5, v6
	v_mov_b32_e32 v4, v2
	s_waitcnt lgkmcnt(0)
	s_nop 1
	v_permlane32_swap_b32_e32 v4, v2
	v_max_f32_e32 v4, v2, v4
	s_cbranch_vccz .Ldf1_first
	v_cmp_lt_f32_e32 vcc, s11, v4
	s_cbranch_vccz .LBB0_839
	v_max_f32_e32 v2, v4, v4
	v_max_f32_e32 v2, 0, v2
	s_branch .Ldf1_resc

.LBB0_883:
	s_mul_i32 s2, s74, 0x4400
	s_add_i32 s83, s2, 0
	v_add_u32_e32 v164, s83, v207
	s_cmp_lg_u32 s82, -1
	ds_read_b128 v[4:7], v164 offset:4608
	ds_read_b128 v[8:11], v164
	ds_read_b128 v[12:15], v164 offset:32
	ds_read_b128 v[146:149], v164 offset:4640
	s_cselect_b64 s[88:89], -1, 0
	v_sub_u32_e32 v2, v177, v176
	v_cmp_gt_i32_e64 s[2:3], v2, 59
	v_cmp_lt_i32_e64 s[6:7], v2, 59
	v_cmp_gt_i32_e64 s[24:25], v2, 18
	s_waitcnt lgkmcnt(2)
	v_mfma_f32_32x32x16_bf16 v[130:145], v[8:11], v[178:181], v[98:113]
	v_cmp_gt_i32_e64 s[26:27], v2, 49
	v_mfma_f32_32x32x16_bf16 v[114:129], v[4:7], v[178:181], v[98:113]
	v_cmp_gt_i32_e64 s[28:29], v2, 17
	v_cmp_gt_i32_e64 s[30:31], v2, 48
	v_cmp_gt_i32_e64 s[34:35], v2, 16
	v_cmp_gt_i32_e64 s[36:37], v2, 43
	v_cmp_gt_i32_e64 s[38:39], v2, 11
	v_cmp_gt_i32_e64 s[40:41], v2, 42
	v_cmp_gt_i32_e64 s[42:43], v2, 10
	s_waitcnt lgkmcnt(1)
	v_mfma_f32_32x32x16_bf16 v[130:145], v[12:15], v[182:185], v[130:145]
	v_cmp_gt_i32_e64 s[44:45], v2, 41
	v_cmp_gt_i32_e64 s[46:47], v2, 9
	v_cmp_gt_i32_e64 s[48:49], v2, 40
	v_cmp_gt_i32_e64 s[50:51], v2, 8
	s_waitcnt lgkmcnt(0)
	v_mfma_f32_32x32x16_bf16 v[114:129], v[146:149], v[182:185], v[114:129]
	v_cmp_gt_i32_e64 s[52:53], v2, 35
	v_cmp_gt_i32_e64 s[54:55], v2, 3
	v_cmp_gt_i32_e64 s[56:57], v2, 34
	v_cmp_gt_i32_e64 s[58:59], v2, 2
	v_cmp_gt_i32_e64 s[8:9], v2, 26
	v_cmp_gt_i32_e64 s[10:11], v2, 57
	v_cmp_gt_i32_e64 s[12:13], v2, 25
	v_cmp_gt_i32_e64 s[14:15], v2, 56
	v_cmp_gt_i32_e64 s[16:17], v2, 24
	v_cmp_gt_i32_e64 s[18:19], v2, 51
	v_cmp_gt_i32_e64 s[20:21], v2, 19
	v_cmp_gt_i32_e64 s[22:23], v2, 50
	v_cmp_gt_i32_e64 s[4:5], v2, 27
	v_cndmask_b32_e64 v4, v130, v243, s[2:3]
	v_cmp_gt_i32_e64 s[60:61], v2, 33
	v_cndmask_b32_e64 v160, v114, v243, s[4:5]
	v_cndmask_b32_e64 v162, v4, v130, s[6:7]
	v_cndmask_b32_e64 v163, v243, v131, s[6:7]
	v_cndmask_b32_e64 v161, v115, v243, s[8:9]
	v_cndmask_b32_e64 v156, v132, v243, s[10:11]
	v_cndmask_b32_e64 v158, v116, v243, s[12:13]
	v_cmp_gt_i32_e64 s[62:63], v2, 1
	v_cndmask_b32_e64 v157, v133, v243, s[14:15]
	v_cndmask_b32_e64 v159, v117, v243, s[16:17]
	v_cndmask_b32_e64 v152, v134, v243, s[18:19]
	v_cndmask_b32_e64 v154, v118, v243, s[20:21]
	v_cmp_gt_i32_e64 s[64:65], v2, 32
	v_max3_f32 v2, v162, v163, v156
	v_max3_f32 v114, v160, v161, v158
	v_cndmask_b32_e64 v153, v135, v243, s[22:23]
	v_cndmask_b32_e64 v155, v119, v243, s[24:25]
	v_cndmask_b32_e64 v148, v136, v243, s[26:27]
	v_cndmask_b32_e64 v150, v120, v243, s[28:29]
	v_max3_f32 v2, v2, v157, v152
	v_max3_f32 v114, v114, v159, v154
	v_cndmask_b32_e64 v149, v137, v243, s[30:31]
	v_cndmask_b32_e64 v151, v121, v243, s[34:35]
	v_cndmask_b32_e64 v10, v138, v243, s[36:37]
	v_cndmask_b32_e64 v146, v122, v243, s[38:39]
	v_max3_f32 v2, v2, v153, v148
	v_max3_f32 v114, v114, v155, v150
	v_cndmask_b32_e64 v11, v139, v243, s[40:41]
	v_cndmask_b32_e64 v147, v123, v243, s[42:43]
	v_cndmask_b32_e64 v8, v140, v243, s[44:45]
	v_cndmask_b32_e64 v12, v124, v243, s[46:47]
	v_cmp_gt_i32_e64 s[66:67], v177, v176
	v_max3_f32 v2, v2, v149, v10
	v_max3_f32 v114, v114, v151, v146
	v_cndmask_b32_e64 v9, v141, v243, s[48:49]
	v_cndmask_b32_e64 v13, v125, v243, s[50:51]
	v_cndmask_b32_e64 v4, v142, v243, s[52:53]
	v_cndmask_b32_e64 v14, v126, v243, s[54:55]
	v_cndmask_b32_e64 v7, v145, v243, s[64:65]
	v_cndmask_b32_e64 v17, v129, v243, s[66:67]
	v_max3_f32 v2, v2, v11, v8
	v_max3_f32 v114, v114, v147, v12
	v_cndmask_b32_e64 v5, v143, v243, s[56:57]
	v_cndmask_b32_e64 v15, v127, v243, s[58:59]
	v_cndmask_b32_e64 v6, v144, v243, s[60:61]
	v_cndmask_b32_e64 v16, v128, v243, s[62:63]
	v_max3_f32 v2, v2, v9, v4
	v_max3_f32 v114, v114, v13, v14
	v_max3_f32 v2, v2, v5, v6
	v_max3_f32 v114, v114, v15, v16
	v_max_f32_e32 v115, v7, v17
	v_max3_f32 v2, v2, v114, v115
	v_mov_b32_e32 v114, v2
	s_and_b64 vcc, exec, s[88:89]
	s_waitcnt lgkmcnt(0)
	s_nop 1
	v_permlane32_swap_b32_e32 v114, v2
	v_max_f32_e32 v114, v2, v114
	s_cbranch_vccz .Ldm0_first
	v_cmp_lt_f32_e32 vcc, s94, v114
	s_mov_b64 s[94:95], s[84:85]
	s_cbranch_vccz .LBB0_890
	v_max_f32_e32 v2, v114, v114
	v_max_f32_e32 v2, 0, v2
	s_branch .Ldm0_resc

.LBB0_890:
	ds_read_b128 v[130:133], v164 offset:64
	ds_read_b128 v[166:169], v164 offset:96
	ds_read_b128 v[170:173], v164 offset:4672
	ds_read_b128 v[194:197], v164 offset:4704
	s_mov_b32 s85, 0x800000
	s_mov_b32 s0, 0x41800000
	s_waitcnt lgkmcnt(3)
	v_mfma_f32_32x32x16_bf16 v[114:129], v[130:133], v[186:189], v[82:97]
	s_waitcnt lgkmcnt(2)
	v_mfma_f32_32x32x16_bf16 v[114:129], v[166:169], v[190:193], v[114:129]
	s_and_b64 vcc, exec, s[88:89]
	s_waitcnt lgkmcnt(1)
	v_mfma_f32_32x32x16_bf16 v[130:145], v[170:173], v[186:189], v[82:97]
	s_nop 8
	v_cndmask_b32_e64 v2, v114, v243, s[2:3]
	v_cndmask_b32_e64 v174, v2, v114, s[6:7]
	v_cndmask_b32_e64 v175, v243, v115, s[6:7]
	v_cndmask_b32_e64 v168, v116, v243, s[10:11]
	v_cndmask_b32_e64 v169, v117, v243, s[14:15]
	v_cndmask_b32_e64 v164, v118, v243, s[18:19]
	v_max3_f32 v2, v174, v175, v168
	s_waitcnt lgkmcnt(0)
	v_mfma_f32_32x32x16_bf16 v[130:145], v[194:197], v[190:193], v[130:145]
	v_cndmask_b32_e64 v165, v119, v243, s[22:23]
	v_max3_f32 v2, v2, v169, v164
	v_cndmask_b32_e64 v124, v124, v243, s[44:45]
	v_cndmask_b32_e64 v125, v125, v243, s[48:49]
	v_cndmask_b32_e64 v115, v129, v243, s[64:65]
	v_cndmask_b32_e64 v114, v128, v243, s[60:61]
	s_nop 5
	v_cndmask_b32_e64 v172, v130, v243, s[4:5]
	v_cndmask_b32_e64 v173, v131, v243, s[8:9]
	v_cndmask_b32_e64 v170, v132, v243, s[12:13]
	v_cndmask_b32_e64 v171, v133, v243, s[16:17]
	v_cndmask_b32_e64 v166, v134, v243, s[20:21]
	v_cndmask_b32_e64 v134, v120, v243, s[26:27]
	v_cndmask_b32_e64 v120, v126, v243, s[52:53]
	v_max3_f32 v126, v172, v173, v170
	v_cndmask_b32_e64 v167, v135, v243, s[24:25]
	v_cndmask_b32_e64 v136, v136, v243, s[28:29]
	v_max3_f32 v126, v126, v171, v166
	v_cndmask_b32_e64 v135, v121, v243, s[30:31]
	v_cndmask_b32_e64 v137, v137, v243, s[34:35]
	v_cndmask_b32_e64 v130, v122, v243, s[36:37]
	v_cndmask_b32_e64 v132, v138, v243, s[38:39]
	v_max3_f32 v2, v2, v165, v134
	v_max3_f32 v126, v126, v167, v136
	v_cndmask_b32_e64 v131, v123, v243, s[40:41]
	v_cndmask_b32_e64 v133, v139, v243, s[42:43]
	v_cndmask_b32_e64 v122, v140, v243, s[46:47]
	v_max3_f32 v2, v2, v135, v130
	v_max3_f32 v126, v126, v137, v132
	v_cndmask_b32_e64 v123, v141, v243, s[50:51]
	v_cndmask_b32_e64 v116, v142, v243, s[54:55]
	v_cndmask_b32_e64 v119, v145, v243, s[66:67]
	v_max3_f32 v2, v2, v131, v124
	v_max3_f32 v126, v126, v133, v122
	v_cndmask_b32_e64 v121, v127, v243, s[56:57]
	v_cndmask_b32_e64 v117, v143, v243, s[58:59]
	v_cndmask_b32_e64 v118, v144, v243, s[62:63]
	v_max3_f32 v2, v2, v125, v120
	v_max3_f32 v126, v126, v123, v116
	v_max3_f32 v2, v2, v121, v114
	v_max3_f32 v126, v126, v117, v118
	v_max_f32_e32 v127, v115, v119
	v_max3_f32 v2, v2, v126, v127
	v_mov_b32_e32 v126, v2
	s_waitcnt lgkmcnt(0)
	s_nop 1
	v_permlane32_swap_b32_e32 v126, v2
	v_max_f32_e32 v126, v2, v126
	s_cbranch_vccz .Ldm1_first
	v_readlane_b32 s56, v255, 12
	v_cmp_lt_f32_e32 vcc, s0, v126
	v_readlane_b32 s57, v255, 13
	s_mov_b32 s55, 0xda24260
	s_cbranch_vccz .LBB0_870
	v_max_f32_e32 v2, v126, v126
	v_max_f32_e32 v2, 0, v2
	s_branch .Ldm1_resc
